# router loop: top-2 merge and weight-sum butterflies over 8-lane groups by DPP moves (quad_perm / row_half_mirror) instead of ds_bpermute round trips
# speedup vs baseline: 1.0075x; 1.0029x over previous
.LBB0_2804:
	s_ashr_i32 s53, s52, 31
	s_lshl_b64 s[8:9], s[52:53], 10
	v_lshl_add_u64 v[12:13], v[10:11], 0, s[8:9]
	v_mul_f32_e32 v12, 0xbfb8aa3b, v40
	v_exp_f32_e32 v12, v12
	s_nop 0
	v_add_f32_e32 v12, 1.0, v12
	v_div_scale_f32 v13, s[8:9], v12, v12, 1.0
	v_rcp_f32_e32 v19, v13
	s_waitcnt lgkmcnt(0)
	v_fma_f32 v20, -v13, v19, 1.0
	v_fmac_f32_e32 v19, v20, v19
	v_div_scale_f32 v20, vcc, 1.0, v12, 1.0
	v_mul_f32_e32 v21, v20, v19
	v_fma_f32 v22, -v13, v21, v20
	v_fmac_f32_e32 v21, v22, v19
	v_fma_f32 v13, -v13, v21, v20
	v_div_fmas_f32 v13, v13, v19, v21
	v_div_fixup_f32 v12, v13, v12, 1.0
	v_mul_f32_e32 v13, 0xbfb8aa3b, v41
	v_exp_f32_e32 v13, v13
	v_add_f32_e32 v21, v4, v12
	v_add_f32_e32 v13, 1.0, v13
	v_div_scale_f32 v19, s[8:9], v13, v13, 1.0
	v_rcp_f32_e32 v20, v19
	s_nop 0
	v_fma_f32 v22, -v19, v20, 1.0
	v_fmac_f32_e32 v20, v22, v20
	v_div_scale_f32 v22, vcc, 1.0, v13, 1.0
	v_mul_f32_e32 v23, v22, v20
	v_fma_f32 v26, -v19, v23, v22
	v_fmac_f32_e32 v23, v26, v20
	v_fma_f32 v19, -v19, v23, v22
	v_div_fmas_f32 v19, v19, v20, v23
	v_div_fixup_f32 v13, v19, v13, 1.0
	v_mul_f32_e32 v19, 0xbfb8aa3b, v42
	v_exp_f32_e32 v19, v19
	v_add_f32_e32 v22, v5, v13
	v_add_f32_e32 v19, 1.0, v19
	v_div_scale_f32 v20, s[8:9], v19, v19, 1.0
	v_rcp_f32_e32 v23, v20
	s_nop 0
	v_fma_f32 v24, -v20, v23, 1.0
	v_fmac_f32_e32 v23, v24, v23
	v_div_scale_f32 v24, vcc, 1.0, v19, 1.0
	v_mul_f32_e32 v26, v24, v23
	v_fma_f32 v27, -v20, v26, v24
	v_fmac_f32_e32 v26, v27, v23
	v_fma_f32 v20, -v20, v26, v24
	v_div_fmas_f32 v20, v20, v23, v26
	v_div_fixup_f32 v19, v20, v19, 1.0
	v_mul_f32_e32 v20, 0xbfb8aa3b, v43
	s_add_i32 s12, s52, s28
	s_cmp_lt_i32 s12, s30
	s_cselect_b32 s12, s12, s52
	s_ashr_i32 s13, s12, 31
	s_lshl_b64 s[12:13], s[12:13], 10
	v_lshl_add_u64 v[44:45], v[10:11], 0, s[12:13]
	global_load_dwordx4 v[40:43], v[44:45], off
	v_exp_f32_e32 v20, v20
	v_add_f32_e32 v23, v6, v19
	v_add_f32_e32 v20, 1.0, v20
	v_div_scale_f32 v24, s[8:9], v20, v20, 1.0
	v_rcp_f32_e32 v25, v24
	s_mov_b32 s8, 0
	v_fma_f32 v26, -v24, v25, 1.0
	v_fmac_f32_e32 v25, v26, v25
	v_div_scale_f32 v26, vcc, 1.0, v20, 1.0
	v_mul_f32_e32 v27, v26, v25
	v_fma_f32 v28, -v24, v27, v26
	v_fmac_f32_e32 v27, v28, v25
	v_fma_f32 v24, -v24, v27, v26
	v_div_fmas_f32 v24, v24, v25, v27
	v_div_fixup_f32 v20, v24, v20, 1.0
	v_add_f32_e32 v25, v7, v20
	v_max_f32_e32 v24, v21, v22
	v_max_f32_e32 v27, v23, v25
	v_min_f32_e32 v26, v21, v22
	v_min_f32_e32 v28, v23, v25
	v_max_f32_e32 v29, v24, v27
	v_min_f32_e32 v24, v24, v27
	v_max3_f32 v24, v24, v26, v28
	s_nop 1
	v_mov_b32_dpp v26, v29 quad_perm:[1,0,3,2] row_mask:0xf bank_mask:0xf
	v_mov_b32_dpp v27, v24 quad_perm:[1,0,3,2] row_mask:0xf bank_mask:0xf
	v_max_f32_e32 v26, v26, v26
	v_max_f32_e32 v28, v29, v26
	v_min_f32_e32 v26, v29, v26
	v_max3_f32 v24, v26, v24, v27
	s_nop 1
	v_mov_b32_dpp v26, v28 quad_perm:[2,3,0,1] row_mask:0xf bank_mask:0xf
	v_mov_b32_dpp v27, v24 quad_perm:[2,3,0,1] row_mask:0xf bank_mask:0xf
	v_max_f32_e32 v26, v26, v26
	v_max_f32_e32 v29, v28, v26
	v_min_f32_e32 v26, v28, v26
	v_max3_f32 v24, v26, v24, v27
	s_nop 1
	v_mov_b32_dpp v26, v29 row_half_mirror row_mask:0xf bank_mask:0xf
	v_mov_b32_dpp v27, v24 row_half_mirror row_mask:0xf bank_mask:0xf
	v_max_f32_e32 v26, v26, v26
	v_max_f32_e32 v28, v29, v26
	v_min_f32_e32 v26, v29, v26
	v_max3_f32 v24, v26, v24, v27
	v_add_f32_e32 v24, v28, v24
	s_nop 0
	v_readlane_b32 s9, v24, 0
	s_nop 1
	v_cmp_eq_f32_e64 s[54:55], s9, v24
	v_cmp_gt_f32_e32 vcc, s9, v24
	s_and_b64 s[12:13], s[36:37], s[54:55]
	v_readlane_b32 s9, v24, 8
	s_or_b64 s[12:13], vcc, s[12:13]
	v_cndmask_b32_e64 v26, 0, 1, s[12:13]
	v_cmp_eq_f32_e64 s[54:55], s9, v24
	v_cmp_gt_f32_e32 vcc, s9, v24
	s_and_b64 s[12:13], s[38:39], s[54:55]
	v_readlane_b32 s9, v24, 16
	s_or_b64 s[12:13], vcc, s[12:13]
	v_cndmask_b32_e64 v27, 0, 1, s[12:13]
	v_cmp_eq_f32_e64 s[54:55], s9, v24
	v_cmp_gt_f32_e32 vcc, s9, v24
	s_and_b64 s[12:13], s[40:41], s[54:55]
	v_readlane_b32 s9, v24, 24
	s_or_b64 s[12:13], vcc, s[12:13]
	v_add_u32_e32 v26, v26, v27
	v_cmp_eq_f32_e64 s[54:55], s9, v24
	v_cndmask_b32_e64 v27, 0, 1, s[12:13]
	v_cmp_gt_f32_e32 vcc, s9, v24
	s_and_b64 s[12:13], s[42:43], s[54:55]
	v_readlane_b32 s9, v24, 32
	s_or_b64 s[12:13], vcc, s[12:13]
	v_cndmask_b32_e64 v28, 0, 1, s[12:13]
	v_cmp_eq_f32_e64 s[54:55], s9, v24
	v_cmp_gt_f32_e32 vcc, s9, v24
	s_and_b64 s[12:13], s[44:45], s[54:55]
	v_readlane_b32 s9, v24, 40
	s_or_b64 s[12:13], vcc, s[12:13]
	v_add3_u32 v26, v26, v27, v28
	v_cmp_eq_f32_e64 s[54:55], s9, v24
	v_cndmask_b32_e64 v27, 0, 1, s[12:13]
	v_cmp_gt_f32_e32 vcc, s9, v24
	s_and_b64 s[12:13], s[46:47], s[54:55]
	v_readlane_b32 s9, v24, 48
	s_or_b64 s[12:13], vcc, s[12:13]
	v_cndmask_b32_e64 v28, 0, 1, s[12:13]
	v_cmp_eq_f32_e64 s[54:55], s9, v24
	v_cmp_gt_f32_e32 vcc, s9, v24
	s_and_b64 s[12:13], s[48:49], s[54:55]
	v_readlane_b32 s9, v24, 56
	s_or_b64 s[12:13], vcc, s[12:13]
	v_add3_u32 v26, v26, v27, v28
	v_cmp_eq_f32_e64 s[54:55], s9, v24
	v_cndmask_b32_e64 v27, 0, 1, s[12:13]
	v_cmp_gt_f32_e32 vcc, s9, v24
	s_and_b64 s[12:13], s[50:51], s[54:55]
	s_or_b64 s[12:13], vcc, s[12:13]
	v_cndmask_b32_e64 v24, 0, 1, s[12:13]
	v_add3_u32 v24, v26, v27, v24
	v_cmp_gt_u32_e32 vcc, 4, v24
	v_mov_b32_e32 v27, 0xf149f2ca
	s_mov_b32 s9, 31
	v_cndmask_b32_e32 v21, v27, v21, vcc
	v_cndmask_b32_e32 v26, v27, v23, vcc
	v_not_b32_e32 v23, v21
	v_or_b32_e32 v24, 0x80000000, v21
	v_cmp_gt_i32_e64 s[54:55], 0, v21
	v_cndmask_b32_e32 v22, v27, v22, vcc
	s_nop 0
	v_cndmask_b32_e64 v21, v24, v23, s[54:55]
	v_cndmask_b32_e32 v24, 0, v21, vcc
	v_not_b32_e32 v21, v22
	v_or_b32_e32 v23, 0x80000000, v22
	v_cmp_gt_i32_e64 s[54:55], 0, v22
	v_or_b32_e32 v22, 0x80000000, v26
	s_nop 0
	v_cndmask_b32_e64 v21, v23, v21, s[54:55]
	v_cndmask_b32_e32 v23, 0, v21, vcc
	v_not_b32_e32 v21, v26
	v_cmp_gt_i32_e64 s[54:55], 0, v26
	s_nop 1
	v_cndmask_b32_e64 v21, v22, v21, s[54:55]
	v_cndmask_b32_e32 v22, 0, v21, vcc
	v_cndmask_b32_e32 v21, v27, v25, vcc
	v_not_b32_e32 v25, v21
	v_cmp_gt_i32_e64 s[54:55], 0, v21
	s_nop 1
	v_cndmask_b32_e64 v21, -|v21|, v25, s[54:55]
	v_cndmask_b32_e32 v21, 0, v21, vcc

.LBB0_2814:
	s_or_b64 exec, exec, s[12:13]
	s_waitcnt lgkmcnt(0)
	v_mov_b32_e32 v13, 0
	v_mov_b32_e32 v12, 0
	s_and_saveexec_b64 s[8:9], s[34:35]
	ds_read2_b32 v[12:13], v18 offset1:8
	s_or_b64 exec, exec, s[8:9]
	s_waitcnt lgkmcnt(0)
	s_nop 4
	v_mov_b32_dpp v19, v13 quad_perm:[1,0,3,2] row_mask:0xf bank_mask:0xf
	v_add_f32_e32 v19, v13, v19
	s_nop 1
	v_mov_b32_dpp v20, v19 quad_perm:[2,3,0,1] row_mask:0xf bank_mask:0xf
	v_add_f32_e32 v19, v19, v20
	s_nop 1
	v_mov_b32_dpp v20, v19 row_half_mirror row_mask:0xf bank_mask:0xf
	s_and_saveexec_b64 s[8:9], s[34:35]
	s_cbranch_execz .LBB0_2803
	s_waitcnt lgkmcnt(0)
	v_add_f32_e32 v19, v19, v20
	v_div_scale_f32 v20, s[12:13], v19, v19, v13
	v_rcp_f32_e32 v21, v20
	v_div_scale_f32 v22, vcc, v13, v19, v13
	v_fma_f32 v23, -v20, v21, 1.0
	v_fmac_f32_e32 v21, v23, v21
	v_mul_f32_e32 v23, v22, v21
	v_fma_f32 v24, -v20, v23, v22
	v_fmac_f32_e32 v23, v24, v21
	v_fma_f32 v20, -v20, v23, v22
	v_div_fmas_f32 v20, v20, v21, v23
	v_div_fixup_f32 v19, v20, v19, v13
	v_ashrrev_i32_e32 v13, 31, v12
	v_lshl_add_u64 v[20:21], v[12:13], 2, s[0:1]
	s_cmp_eq_u32 s100, 0
	s_cbranch_scc1 .Lmy_rt_nopend
	s_waitcnt vmcnt(3)
	global_store_dword v[46:47], v48, off
